# v35
# speedup vs baseline: 1.0257x; 1.0257x over previous
.LBB0_9:
	s_add_i32 s26, s35, 8
	s_cmpk_lt_i32 s26, 0x80
	s_cbranch_scc0 .Lp1_last_top
	s_lshl_b32 s24, s26, 14
	s_add_i32 s24, s24, s33
	s_waitcnt vmcnt(8)
	v_cvt_pk_bf16_f32 v2, v34, v35
	v_cvt_pk_bf16_f32 v3, v36, v37
	v_cvt_pk_bf16_f32 v10, v50, v51
	v_cvt_pk_bf16_f32 v11, v52, v53
	v_cvt_pk_bf16_f32 v4, v38, v39
	v_cvt_pk_bf16_f32 v5, v40, v41
	ds_write2_b64 v212, v[2:3], v[10:11] offset1:68
	v_cvt_pk_bf16_f32 v2, v54, v55
	v_cvt_pk_bf16_f32 v3, v56, v57
	v_cvt_pk_bf16_f32 v6, v42, v43
	v_cvt_pk_bf16_f32 v7, v44, v45
	ds_write2_b64 v215, v[4:5], v[2:3] offset0:16 offset1:84
	v_cvt_pk_bf16_f32 v2, v58, v59
	v_cvt_pk_bf16_f32 v3, v60, v61
	v_cvt_pk_bf16_f32 v8, v46, v47
	v_cvt_pk_bf16_f32 v9, v48, v49
	ds_write2_b64 v216, v[6:7], v[2:3] offset0:32 offset1:100
	v_cvt_pk_bf16_f32 v2, v62, v63
	v_cvt_pk_bf16_f32 v3, v64, v65
	ds_write2_b64 v217, v[8:9], v[2:3] offset0:48 offset1:116
	s_or_b32 s25, s24, 0x1000
	buffer_load_dwordx4 v[34:37], v204, s[12:15], s24 offen sc0 nt sc1
	buffer_load_dwordx4 v[38:41], v204, s[12:15], s25 offen sc0 nt sc1
	s_or_b32 s25, s24, 0x2000
	s_or_b32 s27, s24, 0x3000
	buffer_load_dwordx4 v[42:45], v204, s[12:15], s25 offen sc0 nt sc1
	buffer_load_dwordx4 v[46:49], v204, s[12:15], s27 offen sc0 nt sc1
	s_or_b32 s25, s24, 0x400
	s_or_b32 s27, s24, 0x1400
	buffer_load_dwordx4 v[50:53], v204, s[12:15], s25 offen sc0 nt sc1
	buffer_load_dwordx4 v[54:57], v204, s[12:15], s27 offen sc0 nt sc1
	s_or_b32 s25, s24, 0x2400
	s_or_b32 s27, s24, 0x3400
	buffer_load_dwordx4 v[58:61], v204, s[12:15], s25 offen sc0 nt sc1
	buffer_load_dwordx4 v[62:65], v204, s[12:15], s27 offen sc0 nt sc1
	s_waitcnt vmcnt(8)
	v_cvt_pk_bf16_f32 v2, v66, v67
	v_cvt_pk_bf16_f32 v3, v68, v69
	v_cvt_pk_bf16_f32 v10, v82, v83
	v_cvt_pk_bf16_f32 v11, v84, v85
	v_cvt_pk_bf16_f32 v4, v70, v71
	v_cvt_pk_bf16_f32 v5, v72, v73
	ds_write2_b64 v212, v[2:3], v[10:11] offset0:136 offset1:204
	v_cvt_pk_bf16_f32 v2, v86, v87
	v_cvt_pk_bf16_f32 v3, v88, v89
	v_cvt_pk_bf16_f32 v6, v74, v75
	v_cvt_pk_bf16_f32 v7, v76, v77
	ds_write2_b64 v215, v[4:5], v[2:3] offset0:152 offset1:220
	v_cvt_pk_bf16_f32 v2, v90, v91
	v_cvt_pk_bf16_f32 v3, v92, v93
	v_cvt_pk_bf16_f32 v8, v78, v79
	v_cvt_pk_bf16_f32 v9, v80, v81
	ds_write2_b64 v216, v[6:7], v[2:3] offset0:168 offset1:236
	v_cvt_pk_bf16_f32 v2, v94, v95
	v_cvt_pk_bf16_f32 v3, v96, v97
	ds_write2_b64 v217, v[8:9], v[2:3] offset0:184 offset1:252
	s_or_b32 s25, s24, 0x800
	s_or_b32 s27, s24, 0x1800
	buffer_load_dwordx4 v[66:69], v204, s[12:15], s25 offen sc0 nt sc1
	buffer_load_dwordx4 v[70:73], v204, s[12:15], s27 offen sc0 nt sc1
	s_or_b32 s25, s24, 0x2800
	s_or_b32 s27, s24, 0x3800
	buffer_load_dwordx4 v[74:77], v204, s[12:15], s25 offen sc0 nt sc1
	buffer_load_dwordx4 v[78:81], v204, s[12:15], s27 offen sc0 nt sc1
	s_or_b32 s25, s24, 0xc00
	s_or_b32 s27, s24, 0x1c00
	buffer_load_dwordx4 v[82:85], v204, s[12:15], s25 offen sc0 nt sc1
	buffer_load_dwordx4 v[86:89], v204, s[12:15], s27 offen sc0 nt sc1
	s_or_b32 s25, s24, 0x2c00
	s_or_b32 s24, s24, 0x3c00
	buffer_load_dwordx4 v[90:93], v204, s[12:15], s25 offen sc0 nt sc1
	buffer_load_dwordx4 v[94:97], v204, s[12:15], s24 offen sc0 nt sc1
	s_branch .LBB0_17
